# static s_setprio 1 for waves 4-7 in attention phases 5 and 14 (reset in the grid barrier), on top of hand-written barriers + nt GEMV stream
# speedup vs baseline: 1.0121x; 1.0021x over previous
; __device__ __forceinline__ int lane_id_opaque() { int l; asm volatile("v_mbcnt_lo_u32_b32 %0, -1, 0\n\tv_mbcnt_hi_u32_b32 %0, -1, %0" : "=v"(l)); return l; }
; __device__ __forceinline__ unsigned xb_add(unsigned* p, unsigned v) { return __hip_atomic_fetch_add(p, v, __ATOMIC_RELAXED, __HIP_MEMORY_SCOPE_AGENT); }
; __device__ __forceinline__ void xcd_barrier(const XcdBarrier& b, int wave) {
;     asm volatile("s_waitcnt vmcnt(0)" ::: "memory");
;     __syncthreads();
;     if (wave == 0 && lane_id_opaque() == 0) {
;         unsigned* bar = b.bar;
;         __builtin_amdgcn_s_waitcnt(0);
;         unsigned nloc = b.st[0], nx = b.st[1];
;         if (nloc == 0u) { xcd_barrier_complete(bar, b.x, nloc, nx); b.st[0] = nloc; b.st[1] = nx; }
;         const unsigned old = xb_add(&bar[XB_XSUB(b.x)], 1u);
.LBB0_208:
	s_cmp_gt_u32 s89, 2
	s_cselect_b64 s[0:1], -1, 0
	s_and_b64 s[0:1], s[4:5], s[0:1]
	s_andn2_b64 vcc, exec, s[0:1]
	s_cbranch_vccnz .LBB0_264
	s_setprio 0
	s_waitcnt vmcnt(0) lgkmcnt(0)
	s_barrier
	v_readlane_b32 s0, v254, 45
	s_nop 3
	s_cmp_lg_u32 s0, 0
	s_cbranch_scc1 .Lgb2_end
	s_mov_b64 exec, 1
	v_mov_b32_e32 v0, 0x24160
	ds_read_b64 v[0:1], v0
	v_readlane_b32 s1, v254, 25
	v_readlane_b32 s8, v254, 23
	v_readlane_b32 s9, v254, 24
	s_nop 3
	s_lshl_b32 s1, s1, 8
	s_add_u32 s10, s8, s1
	s_addc_u32 s11, s9, 0
	v_mov_b32_e32 v2, 0x1000
	v_mov_b32_e32 v3, 1
	global_atomic_add v4, v2, v3, s[10:11] offset:1024 sc0
	s_waitcnt vmcnt(0) lgkmcnt(0)
	v_readfirstlane_b32 s12, v4
	v_readfirstlane_b32 s13, v0
	v_readfirstlane_b32 s14, v1
	s_nop 3
	s_mov_b32 s15, 0
	s_max_u32 s13, s13, 1
	s_max_u32 s14, s14, 1

; __device__ __forceinline__ int lane_id_opaque() { int l; asm volatile("v_mbcnt_lo_u32_b32 %0, -1, 0\n\tv_mbcnt_hi_u32_b32 %0, -1, %0" : "=v"(l)); return l; }
; __device__ __forceinline__ unsigned xb_add(unsigned* p, unsigned v) { return __hip_atomic_fetch_add(p, v, __ATOMIC_RELAXED, __HIP_MEMORY_SCOPE_AGENT); }
; __device__ __forceinline__ void xcd_barrier(const XcdBarrier& b, int wave) {
;     asm volatile("s_waitcnt vmcnt(0)" ::: "memory");
;     __syncthreads();
;     if (wave == 0 && lane_id_opaque() == 0) {
;         unsigned* bar = b.bar;
;         __builtin_amdgcn_s_waitcnt(0);
;         unsigned nloc = b.st[0], nx = b.st[1];
;         if (nloc == 0u) { xcd_barrier_complete(bar, b.x, nloc, nx); b.st[0] = nloc; b.st[1] = nx; }
;         const unsigned old = xb_add(&bar[XB_XSUB(b.x)], 1u);
.LBB0_356:
	s_cmp_gt_i32 s89, 4
	s_cselect_b64 s[2:3], -1, 0
	s_and_b64 s[0:1], s[8:9], s[2:3]
	s_andn2_b64 vcc, exec, s[0:1]
	s_cbranch_vccnz .LBB0_412
	s_setprio 0
	s_waitcnt vmcnt(0) lgkmcnt(0)
	s_barrier
	v_readlane_b32 s0, v254, 45
	s_nop 3
	s_cmp_lg_u32 s0, 0
	s_cbranch_scc1 .Lgb4_end
	s_mov_b64 exec, 1
	v_mov_b32_e32 v0, 0x24160
	ds_read_b64 v[0:1], v0
	v_readlane_b32 s1, v254, 25
	v_readlane_b32 s8, v254, 23
	v_readlane_b32 s9, v254, 24
	s_nop 3
	s_lshl_b32 s1, s1, 8
	s_add_u32 s10, s8, s1
	s_addc_u32 s11, s9, 0
	v_mov_b32_e32 v2, 0x1000
	v_mov_b32_e32 v3, 1
	global_atomic_add v4, v2, v3, s[10:11] offset:1024 sc0
	s_waitcnt vmcnt(0) lgkmcnt(0)
	v_readfirstlane_b32 s12, v4
	v_readfirstlane_b32 s13, v0
	v_readfirstlane_b32 s14, v1
	s_nop 3
	s_mov_b32 s15, 0
	s_max_u32 s13, s13, 1
	s_max_u32 s14, s14, 1

; __device__ __forceinline__ int lane_id_opaque() { int l; asm volatile("v_mbcnt_lo_u32_b32 %0, -1, 0\n\tv_mbcnt_hi_u32_b32 %0, -1, %0" : "=v"(l)); return l; }
; __device__ __forceinline__ unsigned xb_add(unsigned* p, unsigned v) { return __hip_atomic_fetch_add(p, v, __ATOMIC_RELAXED, __HIP_MEMORY_SCOPE_AGENT); }
; __device__ __forceinline__ void xcd_barrier(const XcdBarrier& b, int wave) {
;     asm volatile("s_waitcnt vmcnt(0)" ::: "memory");
;     __syncthreads();
;     if (wave == 0 && lane_id_opaque() == 0) {
;         unsigned* bar = b.bar;
;         __builtin_amdgcn_s_waitcnt(0);
;         unsigned nloc = b.st[0], nx = b.st[1];
;         if (nloc == 0u) { xcd_barrier_complete(bar, b.x, nloc, nx); b.st[0] = nloc; b.st[1] = nx; }
;         const unsigned old = xb_add(&bar[XB_XSUB(b.x)], 1u);
.LBB0_451:
	s_cmp_gt_i32 s89, 5
	s_cselect_b64 s[2:3], -1, 0
	s_and_b64 s[0:1], s[6:7], s[2:3]
	s_andn2_b64 vcc, exec, s[0:1]
	s_cbranch_vccnz .LBB0_507
	s_setprio 0
	s_waitcnt vmcnt(0) lgkmcnt(0)
	s_barrier
	v_readlane_b32 s0, v254, 45
	s_nop 3
	s_cmp_lg_u32 s0, 0
	s_cbranch_scc1 .Lgb5_end
	s_mov_b64 exec, 1
	v_mov_b32_e32 v0, 0x24160
	ds_read_b64 v[0:1], v0
	v_readlane_b32 s1, v254, 25
	v_readlane_b32 s8, v254, 23
	v_readlane_b32 s9, v254, 24
	s_nop 3
	s_lshl_b32 s1, s1, 8
	s_add_u32 s10, s8, s1
	s_addc_u32 s11, s9, 0
	v_mov_b32_e32 v2, 0x1000
	v_mov_b32_e32 v3, 1
	global_atomic_add v4, v2, v3, s[10:11] offset:1024 sc0
	s_waitcnt vmcnt(0) lgkmcnt(0)
	v_readfirstlane_b32 s12, v4
	v_readfirstlane_b32 s13, v0
	v_readfirstlane_b32 s14, v1
	s_nop 3
	s_mov_b32 s15, 0
	s_max_u32 s13, s13, 1
	s_max_u32 s14, s14, 1

; #define LAS __attribute__((address_space(3)))
; __device__ __forceinline__ int lane_id_opaque() { int l; asm volatile("v_mbcnt_lo_u32_b32 %0, -1, 0\n\tv_mbcnt_hi_u32_b32 %0, -1, %0" : "=v"(l)); return l; }
; #define PHASE_IDS(F) const int lane = lane_id_opaque(), wave = (F).wave, tid = wave * 64 + lane; (void)lane; (void)wave; (void)tid
; #define REP(k) _Pragma("unroll 1") for (int rep_ = 0; rep_ < ((((PH_DUP) >> (k)) & 1u) ? 2 : 1); ++rep_)
; #define SEAM(k) do { PH_IDLE(k); if (IN(k) && IN((k) + 1)) xcd_barrier(bar, F.wave); PH_MARK(); } while (0)
; __device__ __forceinline__ void router_pre(Frame& F, const Args& A, int layer, int b) {
;     PHASE_IDS(F);
;     const float* MOD = (const float*)(F.ctl + CW_MOD); const int jn = 2 * layer + 1;
;     const float* shp = MOD + (size_t)(jn * 4 + b) * 6144; const float* scp = shp + 2048; const float* gvec = A.in[8] + layer * 2048;
;     const f32x4* WR4 = (const f32x4*)(F.ws + WS_WR) + (size_t)layer * 512 * 36;
;     float* QV = (float*)(F.ws + WS_RQ) + (layer * 4 + b) * 36; float* GS = (float*)(F.ws + WS_RQ + 4096) + (size_t)(layer * 4 + b) * 2048;
;     LAS float* qq = (LAS float*)(F.lds + RING_OFF);
;     for (int k = tid; k < 2048; k += 512) GS[k] = gvec[k] * (1.0f + scp[k]);
; __global__ void __launch_bounds__(NWAVES * 64, 2) mk_fwd(Args args) {
;     ...
;     if (IN(5)) REP(5) { if (F.vcu < 8) router_pre(F, args, F.vcu >> 2, F.vcu & 3);
;         bool conv_left = true; WorkQ QC; wq_init(F, QC, F.ctl + CW_QC1, CONV_N1 / 64, 18, lane_id_opaque()); mla_phase(F, args, QC, conv_left); sb_phase(F, args, QC, conv_left); } SEAM(5);
.LBB0_507:
	s_cmp_lt_i32 s88, 6
	s_cselect_b64 s[0:1], -1, 0
	s_add_u32 s4, s50, 0x10000
	s_addc_u32 s5, s51, 0
	v_writelane_b32 v254, s4, 50
	s_and_b64 s[70:71], s[0:1], s[2:3]
	s_andn2_b64 vcc, exec, s[70:71]
	v_writelane_b32 v254, s5, 51
	v_writelane_b32 v254, s92, 52
	s_cbranch_vccnz .LBB0_1473
	v_readlane_b32 s0, v254, 45
	s_nop 3
	s_cmp_lt_u32 s0, 4
	s_cbranch_scc1 .Lprio_p9597
	s_setprio 1
.Lprio_p9597:
	v_readlane_b32 s0, v254, 4
	s_andn2_b32 s0, s0, 63
	s_cmp_gt_i32 s86, 7
	v_writelane_b32 v254, s0, 53
	s_cbranch_scc1 .LBB0_596
	s_ashr_i32 s2, s86, 2
	v_readlane_b32 s3, v254, 53
	s_lshl_b32 s10, s2, 11
	v_mbcnt_lo_u32_b32 v152, -1, 0
	v_mbcnt_hi_u32_b32 v152, -1, v152
	s_and_b32 s0, s86, 3
	v_add_u32_e32 v144, s3, v152
	s_movk_i32 s3, 0x800
	s_lshl_b32 s1, s2, 3
	s_ashr_i32 s11, s10, 31
	s_ashr_i32 s87, s86, 31
	v_cmp_gt_i32_e32 vcc, s3, v144
	v_ashrrev_i32_e32 v145, 31, v144
	s_and_saveexec_b64 s[4:5], vcc
	s_cbranch_execz .LBB0_512
	s_lshl_b64 s[6:7], s[86:87], 13
	s_lshl_b64 s[8:9], s[10:11], 2
	s_add_u32 s8, s68, s8
	s_addc_u32 s9, s69, s9
	s_add_u32 s6, s50, s6
	s_waitcnt vmcnt(0)
	v_lshlrev_b64 v[4:5], 2, v[144:145]
	s_addc_u32 s7, s51, s7
	s_add_i32 s3, s1, s0
	s_waitcnt lgkmcnt(0)
	v_lshl_add_u64 v[2:3], s[6:7], 0, v[4:5]
	s_mov_b64 s[6:7], 0xcc1000
	s_add_i32 s3, s3, 4
	v_lshl_add_u64 v[2:3], v[2:3], 0, s[6:7]
	s_mul_hi_i32 s7, s3, 0x6000
	s_mulk_i32 s3, 0x6000
	s_add_u32 s6, s50, s3
	s_addc_u32 s7, s51, s7
	v_lshl_add_u64 v[0:1], s[8:9], 0, v[4:5]
	v_lshl_add_u64 v[4:5], s[6:7], 0, v[4:5]
	s_mov_b64 s[6:7], 0x12000
	v_add_u32_e32 v6, 0xfffffe00, v144
	v_lshl_add_u64 v[4:5], v[4:5], 0, s[6:7]
	s_mov_b64 s[6:7], 0
	s_mov_b64 s[8:9], 0x800
	s_movk_i32 s3, 0x5ff

; __device__ __forceinline__ int lane_id_opaque() { int l; asm volatile("v_mbcnt_lo_u32_b32 %0, -1, 0\n\tv_mbcnt_hi_u32_b32 %0, -1, %0" : "=v"(l)); return l; }
; __device__ __forceinline__ unsigned xb_add(unsigned* p, unsigned v) { return __hip_atomic_fetch_add(p, v, __ATOMIC_RELAXED, __HIP_MEMORY_SCOPE_AGENT); }
; __device__ __forceinline__ void xcd_barrier(const XcdBarrier& b, int wave) {
;     asm volatile("s_waitcnt vmcnt(0)" ::: "memory");
;     __syncthreads();
;     if (wave == 0 && lane_id_opaque() == 0) {
;         unsigned* bar = b.bar;
;         __builtin_amdgcn_s_waitcnt(0);
;         unsigned nloc = b.st[0], nx = b.st[1];
;         if (nloc == 0u) { xcd_barrier_complete(bar, b.x, nloc, nx); b.st[0] = nloc; b.st[1] = nx; }
;         const unsigned old = xb_add(&bar[XB_XSUB(b.x)], 1u);
.LBB0_1473:
	s_cmp_gt_i32 s89, 6
	s_cselect_b64 s[2:3], -1, 0
	s_and_b64 s[0:1], s[70:71], s[2:3]
	s_andn2_b64 vcc, exec, s[0:1]
	s_cbranch_vccnz .LBB0_1529
	s_setprio 0
	s_waitcnt vmcnt(0) lgkmcnt(0)
	s_barrier
	v_readlane_b32 s0, v254, 45
	s_nop 3
	s_cmp_lg_u32 s0, 0
	s_cbranch_scc1 .Lgb6_end
	s_mov_b64 exec, 1
	v_mov_b32_e32 v0, 0x24160
	ds_read_b64 v[0:1], v0
	v_readlane_b32 s1, v254, 25
	v_readlane_b32 s8, v254, 23
	v_readlane_b32 s9, v254, 24
	s_nop 3
	s_lshl_b32 s1, s1, 8
	s_add_u32 s10, s8, s1
	s_addc_u32 s11, s9, 0
	v_mov_b32_e32 v2, 0x1000
	v_mov_b32_e32 v3, 1
	global_atomic_add v4, v2, v3, s[10:11] offset:1024 sc0
	s_waitcnt vmcnt(0) lgkmcnt(0)
	v_readfirstlane_b32 s12, v4
	v_readfirstlane_b32 s13, v0
	v_readfirstlane_b32 s14, v1
	s_nop 3
	s_mov_b32 s15, 0
	s_max_u32 s13, s13, 1
	s_max_u32 s14, s14, 1

; __device__ __forceinline__ int lane_id_opaque() { int l; asm volatile("v_mbcnt_lo_u32_b32 %0, -1, 0\n\tv_mbcnt_hi_u32_b32 %0, -1, %0" : "=v"(l)); return l; }
; __device__ __forceinline__ unsigned xb_add(unsigned* p, unsigned v) { return __hip_atomic_fetch_add(p, v, __ATOMIC_RELAXED, __HIP_MEMORY_SCOPE_AGENT); }
; __device__ __forceinline__ void xcd_barrier(const XcdBarrier& b, int wave) {
;     asm volatile("s_waitcnt vmcnt(0)" ::: "memory");
;     __syncthreads();
;     if (wave == 0 && lane_id_opaque() == 0) {
;         unsigned* bar = b.bar;
;         __builtin_amdgcn_s_waitcnt(0);
;         unsigned nloc = b.st[0], nx = b.st[1];
;         if (nloc == 0u) { xcd_barrier_complete(bar, b.x, nloc, nx); b.st[0] = nloc; b.st[1] = nx; }
;         const unsigned old = xb_add(&bar[XB_XSUB(b.x)], 1u);
.LBB0_1550:
	s_cmp_gt_i32 s89, 7
	s_cselect_b64 s[2:3], -1, 0
	s_and_b64 s[0:1], s[4:5], s[2:3]
	s_andn2_b64 vcc, exec, s[0:1]
	s_cbranch_vccnz .LBB0_1606
	s_setprio 0
	s_waitcnt vmcnt(0) lgkmcnt(0)
	s_barrier
	v_readlane_b32 s0, v254, 45
	s_nop 3
	s_cmp_lg_u32 s0, 0
	s_cbranch_scc1 .Lgb7_end
	s_mov_b64 exec, 1
	v_mov_b32_e32 v0, 0x24160
	ds_read_b64 v[0:1], v0
	v_readlane_b32 s1, v254, 25
	v_readlane_b32 s8, v254, 23
	v_readlane_b32 s9, v254, 24
	s_nop 3
	s_lshl_b32 s1, s1, 8
	s_add_u32 s10, s8, s1
	s_addc_u32 s11, s9, 0
	v_mov_b32_e32 v2, 0x1000
	v_mov_b32_e32 v3, 1
	global_atomic_add v4, v2, v3, s[10:11] offset:1024 sc0
	s_waitcnt vmcnt(0) lgkmcnt(0)
	v_readfirstlane_b32 s12, v4
	v_readfirstlane_b32 s13, v0
	v_readfirstlane_b32 s14, v1
	s_nop 3
	s_mov_b32 s15, 0
	s_max_u32 s13, s13, 1
	s_max_u32 s14, s14, 1

; __device__ __forceinline__ int lane_id_opaque() { int l; asm volatile("v_mbcnt_lo_u32_b32 %0, -1, 0\n\tv_mbcnt_hi_u32_b32 %0, -1, %0" : "=v"(l)); return l; }
; __device__ __forceinline__ unsigned xb_add(unsigned* p, unsigned v) { return __hip_atomic_fetch_add(p, v, __ATOMIC_RELAXED, __HIP_MEMORY_SCOPE_AGENT); }
; __device__ __forceinline__ void xcd_barrier(const XcdBarrier& b, int wave) {
;     asm volatile("s_waitcnt vmcnt(0)" ::: "memory");
;     __syncthreads();
;     if (wave == 0 && lane_id_opaque() == 0) {
;         unsigned* bar = b.bar;
;         __builtin_amdgcn_s_waitcnt(0);
;         unsigned nloc = b.st[0], nx = b.st[1];
;         if (nloc == 0u) { xcd_barrier_complete(bar, b.x, nloc, nx); b.st[0] = nloc; b.st[1] = nx; }
;         const unsigned old = xb_add(&bar[XB_XSUB(b.x)], 1u);
.LBB0_1664:
	s_cmp_gt_i32 s89, 8
	s_cselect_b64 s[2:3], -1, 0
	s_and_b64 s[0:1], s[26:27], s[2:3]
	s_andn2_b64 vcc, exec, s[0:1]
	s_cbranch_vccnz .LBB0_1720
	s_setprio 0
	s_waitcnt vmcnt(0) lgkmcnt(0)
	s_barrier
	v_readlane_b32 s0, v254, 45
	s_nop 3
	s_cmp_lg_u32 s0, 0
	s_cbranch_scc1 .Lgb8_end
	s_mov_b64 exec, 1
	v_mov_b32_e32 v0, 0x24160
	ds_read_b64 v[0:1], v0
	v_readlane_b32 s1, v254, 25
	v_readlane_b32 s8, v254, 23
	v_readlane_b32 s9, v254, 24
	s_nop 3
	s_lshl_b32 s1, s1, 8
	s_add_u32 s10, s8, s1
	s_addc_u32 s11, s9, 0
	v_mov_b32_e32 v2, 0x1000
	v_mov_b32_e32 v3, 1
	global_atomic_add v4, v2, v3, s[10:11] offset:1024 sc0
	s_waitcnt vmcnt(0) lgkmcnt(0)
	v_readfirstlane_b32 s12, v4
	v_readfirstlane_b32 s13, v0
	v_readfirstlane_b32 s14, v1
	s_nop 3
	s_mov_b32 s15, 0
	s_max_u32 s13, s13, 1
	s_max_u32 s14, s14, 1

; __device__ __forceinline__ int lane_id_opaque() { int l; asm volatile("v_mbcnt_lo_u32_b32 %0, -1, 0\n\tv_mbcnt_hi_u32_b32 %0, -1, %0" : "=v"(l)); return l; }
; __device__ __forceinline__ unsigned xb_add(unsigned* p, unsigned v) { return __hip_atomic_fetch_add(p, v, __ATOMIC_RELAXED, __HIP_MEMORY_SCOPE_AGENT); }
; __device__ __forceinline__ void xcd_barrier(const XcdBarrier& b, int wave) {
;     asm volatile("s_waitcnt vmcnt(0)" ::: "memory");
;     __syncthreads();
;     if (wave == 0 && lane_id_opaque() == 0) {
;         unsigned* bar = b.bar;
;         __builtin_amdgcn_s_waitcnt(0);
;         unsigned nloc = b.st[0], nx = b.st[1];
;         if (nloc == 0u) { xcd_barrier_complete(bar, b.x, nloc, nx); b.st[0] = nloc; b.st[1] = nx; }
;         const unsigned old = xb_add(&bar[XB_XSUB(b.x)], 1u);
.LBB0_1753:
	s_cmp_gt_i32 s89, 9
	s_cselect_b64 s[4:5], -1, 0
	s_and_b64 s[0:1], s[6:7], s[4:5]
	s_andn2_b64 vcc, exec, s[0:1]
	s_cbranch_vccnz .LBB0_1809
	s_setprio 0
	s_waitcnt vmcnt(0) lgkmcnt(0)
	s_barrier
	v_readlane_b32 s0, v254, 45
	s_nop 3
	s_cmp_lg_u32 s0, 0
	s_cbranch_scc1 .Lgb9_end
	s_mov_b64 exec, 1
	v_mov_b32_e32 v0, 0x24160
	ds_read_b64 v[0:1], v0
	v_readlane_b32 s1, v254, 25
	v_readlane_b32 s8, v254, 23
	v_readlane_b32 s9, v254, 24
	s_nop 3
	s_lshl_b32 s1, s1, 8
	s_add_u32 s10, s8, s1
	s_addc_u32 s11, s9, 0
	v_mov_b32_e32 v2, 0x1000
	v_mov_b32_e32 v3, 1
	global_atomic_add v4, v2, v3, s[10:11] offset:1024 sc0
	s_waitcnt vmcnt(0) lgkmcnt(0)
	v_readfirstlane_b32 s12, v4
	v_readfirstlane_b32 s13, v0
	v_readfirstlane_b32 s14, v1
	s_nop 3
	s_mov_b32 s15, 0
	s_max_u32 s13, s13, 1
	s_max_u32 s14, s14, 1

; __device__ __forceinline__ int lane_id_opaque() { int l; asm volatile("v_mbcnt_lo_u32_b32 %0, -1, 0\n\tv_mbcnt_hi_u32_b32 %0, -1, %0" : "=v"(l)); return l; }
; __device__ __forceinline__ unsigned xb_add(unsigned* p, unsigned v) { return __hip_atomic_fetch_add(p, v, __ATOMIC_RELAXED, __HIP_MEMORY_SCOPE_AGENT); }
; __device__ __forceinline__ void xcd_barrier(const XcdBarrier& b, int wave) {
;     asm volatile("s_waitcnt vmcnt(0)" ::: "memory");
;     __syncthreads();
;     if (wave == 0 && lane_id_opaque() == 0) {
;         unsigned* bar = b.bar;
;         __builtin_amdgcn_s_waitcnt(0);
;         unsigned nloc = b.st[0], nx = b.st[1];
;         if (nloc == 0u) { xcd_barrier_complete(bar, b.x, nloc, nx); b.st[0] = nloc; b.st[1] = nx; }
;         const unsigned old = xb_add(&bar[XB_XSUB(b.x)], 1u);
.LBB0_1826:
	s_cmp_gt_i32 s89, 10
	s_cselect_b64 s[4:5], -1, 0
	s_and_b64 s[0:1], s[2:3], s[4:5]
	s_andn2_b64 vcc, exec, s[0:1]
	s_cbranch_vccnz .LBB0_1882
	s_setprio 0
	s_waitcnt vmcnt(0) lgkmcnt(0)
	s_barrier
	v_readlane_b32 s0, v254, 45
	s_nop 3
	s_cmp_lg_u32 s0, 0
	s_cbranch_scc1 .Lgb10_end
	s_mov_b64 exec, 1
	v_mov_b32_e32 v0, 0x24160
	ds_read_b64 v[0:1], v0
	v_readlane_b32 s1, v254, 25
	v_readlane_b32 s8, v254, 23
	v_readlane_b32 s9, v254, 24
	s_nop 3
	s_lshl_b32 s1, s1, 8
	s_add_u32 s10, s8, s1
	s_addc_u32 s11, s9, 0
	v_mov_b32_e32 v2, 0x1000
	v_mov_b32_e32 v3, 1
	global_atomic_add v4, v2, v3, s[10:11] offset:1024 sc0
	s_waitcnt vmcnt(0) lgkmcnt(0)
	v_readfirstlane_b32 s12, v4
	v_readfirstlane_b32 s13, v0
	v_readfirstlane_b32 s14, v1
	s_nop 3
	s_mov_b32 s15, 0
	s_max_u32 s13, s13, 1
	s_max_u32 s14, s14, 1

; __device__ __forceinline__ int lane_id_opaque() { int l; asm volatile("v_mbcnt_lo_u32_b32 %0, -1, 0\n\tv_mbcnt_hi_u32_b32 %0, -1, %0" : "=v"(l)); return l; }
; __device__ __forceinline__ unsigned xb_add(unsigned* p, unsigned v) { return __hip_atomic_fetch_add(p, v, __ATOMIC_RELAXED, __HIP_MEMORY_SCOPE_AGENT); }
; __device__ __forceinline__ void xcd_barrier(const XcdBarrier& b, int wave) {
;     asm volatile("s_waitcnt vmcnt(0)" ::: "memory");
;     __syncthreads();
;     if (wave == 0 && lane_id_opaque() == 0) {
;         unsigned* bar = b.bar;
;         __builtin_amdgcn_s_waitcnt(0);
;         unsigned nloc = b.st[0], nx = b.st[1];
;         if (nloc == 0u) { xcd_barrier_complete(bar, b.x, nloc, nx); b.st[0] = nloc; b.st[1] = nx; }
;         const unsigned old = xb_add(&bar[XB_XSUB(b.x)], 1u);
.LBB0_1936:
	s_cmp_gt_i32 s89, 11
	s_cselect_b64 s[4:5], -1, 0
	s_and_b64 s[0:1], s[2:3], s[4:5]
	s_andn2_b64 vcc, exec, s[0:1]
	s_cbranch_vccnz .LBB0_1992
	s_setprio 0
	s_waitcnt vmcnt(0) lgkmcnt(0)
	s_barrier
	v_readlane_b32 s0, v254, 45
	s_nop 3
	s_cmp_lg_u32 s0, 0
	s_cbranch_scc1 .Lgb11_end
	s_mov_b64 exec, 1
	v_mov_b32_e32 v0, 0x24160
	ds_read_b64 v[0:1], v0
	v_readlane_b32 s1, v254, 25
	v_readlane_b32 s8, v254, 23
	v_readlane_b32 s9, v254, 24
	s_nop 3
	s_lshl_b32 s1, s1, 8
	s_add_u32 s10, s8, s1
	s_addc_u32 s11, s9, 0
	v_mov_b32_e32 v2, 0x1000
	v_mov_b32_e32 v3, 1
	global_atomic_add v4, v2, v3, s[10:11] offset:1024 sc0
	s_waitcnt vmcnt(0) lgkmcnt(0)
	v_readfirstlane_b32 s12, v4
	v_readfirstlane_b32 s13, v0
	v_readfirstlane_b32 s14, v1
	s_nop 3
	s_mov_b32 s15, 0
	s_max_u32 s13, s13, 1
	s_max_u32 s14, s14, 1

; __device__ __forceinline__ int lane_id_opaque() { int l; asm volatile("v_mbcnt_lo_u32_b32 %0, -1, 0\n\tv_mbcnt_hi_u32_b32 %0, -1, %0" : "=v"(l)); return l; }
; __device__ __forceinline__ unsigned xb_add(unsigned* p, unsigned v) { return __hip_atomic_fetch_add(p, v, __ATOMIC_RELAXED, __HIP_MEMORY_SCOPE_AGENT); }
; __device__ __forceinline__ void xcd_barrier(const XcdBarrier& b, int wave) {
;     asm volatile("s_waitcnt vmcnt(0)" ::: "memory");
;     __syncthreads();
;     if (wave == 0 && lane_id_opaque() == 0) {
;         unsigned* bar = b.bar;
;         __builtin_amdgcn_s_waitcnt(0);
;         unsigned nloc = b.st[0], nx = b.st[1];
;         if (nloc == 0u) { xcd_barrier_complete(bar, b.x, nloc, nx); b.st[0] = nloc; b.st[1] = nx; }
;         const unsigned old = xb_add(&bar[XB_XSUB(b.x)], 1u);
.LBB0_2009:
	s_cmp_gt_i32 s89, 12
	s_cselect_b64 s[6:7], -1, 0
	s_and_b64 s[0:1], s[2:3], s[6:7]
	s_andn2_b64 vcc, exec, s[0:1]
	s_cbranch_vccnz .LBB0_2065
	s_setprio 0
	s_waitcnt vmcnt(0) lgkmcnt(0)
	s_barrier
	v_readlane_b32 s0, v254, 45
	s_nop 3
	s_cmp_lg_u32 s0, 0
	s_cbranch_scc1 .Lgb12_end
	s_mov_b64 exec, 1
	v_mov_b32_e32 v0, 0x24160
	ds_read_b64 v[0:1], v0
	v_readlane_b32 s1, v254, 25
	v_readlane_b32 s8, v254, 23
	v_readlane_b32 s9, v254, 24
	s_nop 3
	s_lshl_b32 s1, s1, 8
	s_add_u32 s10, s8, s1
	s_addc_u32 s11, s9, 0
	v_mov_b32_e32 v2, 0x1000
	v_mov_b32_e32 v3, 1
	global_atomic_add v4, v2, v3, s[10:11] offset:1024 sc0
	s_waitcnt vmcnt(0) lgkmcnt(0)
	v_readfirstlane_b32 s12, v4
	v_readfirstlane_b32 s13, v0
	v_readfirstlane_b32 s14, v1
	s_nop 3
	s_mov_b32 s15, 0
	s_max_u32 s13, s13, 1
	s_max_u32 s14, s14, 1

; __device__ __forceinline__ int lane_id_opaque() { int l; asm volatile("v_mbcnt_lo_u32_b32 %0, -1, 0\n\tv_mbcnt_hi_u32_b32 %0, -1, %0" : "=v"(l)); return l; }
; __device__ __forceinline__ unsigned xb_add(unsigned* p, unsigned v) { return __hip_atomic_fetch_add(p, v, __ATOMIC_RELAXED, __HIP_MEMORY_SCOPE_AGENT); }
; __device__ __forceinline__ void xcd_barrier(const XcdBarrier& b, int wave) {
;     asm volatile("s_waitcnt vmcnt(0)" ::: "memory");
;     __syncthreads();
;     if (wave == 0 && lane_id_opaque() == 0) {
;         unsigned* bar = b.bar;
;         __builtin_amdgcn_s_waitcnt(0);
;         unsigned nloc = b.st[0], nx = b.st[1];
;         if (nloc == 0u) { xcd_barrier_complete(bar, b.x, nloc, nx); b.st[0] = nloc; b.st[1] = nx; }
;         const unsigned old = xb_add(&bar[XB_XSUB(b.x)], 1u);
.LBB0_2075:
	s_cmp_gt_i32 s89, 13
	s_cselect_b64 s[2:3], -1, 0
	s_and_b64 s[0:1], s[4:5], s[2:3]
	s_andn2_b64 vcc, exec, s[0:1]
	s_cbranch_vccnz .LBB0_2131
	s_setprio 0
	s_waitcnt vmcnt(0) lgkmcnt(0)
	s_barrier
	v_readlane_b32 s0, v254, 45
	s_nop 3
	s_cmp_lg_u32 s0, 0
	s_cbranch_scc1 .Lgb13_end
	s_mov_b64 exec, 1
	v_mov_b32_e32 v0, 0x24160
	ds_read_b64 v[0:1], v0
	v_readlane_b32 s1, v254, 25
	v_readlane_b32 s8, v254, 23
	v_readlane_b32 s9, v254, 24
	s_nop 3
	s_lshl_b32 s1, s1, 8
	s_add_u32 s10, s8, s1
	s_addc_u32 s11, s9, 0
	v_mov_b32_e32 v2, 0x1000
	v_mov_b32_e32 v3, 1
	global_atomic_add v4, v2, v3, s[10:11] offset:1024 sc0
	s_waitcnt vmcnt(0) lgkmcnt(0)
	v_readfirstlane_b32 s12, v4
	v_readfirstlane_b32 s13, v0
	v_readfirstlane_b32 s14, v1
	s_nop 3
	s_mov_b32 s15, 0
	s_max_u32 s13, s13, 1
	s_max_u32 s14, s14, 1

; __device__ __forceinline__ int lane_id_opaque() { int l; asm volatile("v_mbcnt_lo_u32_b32 %0, -1, 0\n\tv_mbcnt_hi_u32_b32 %0, -1, %0" : "=v"(l)); return l; }
; __device__ __forceinline__ unsigned xb_add(unsigned* p, unsigned v) { return __hip_atomic_fetch_add(p, v, __ATOMIC_RELAXED, __HIP_MEMORY_SCOPE_AGENT); }
; __device__ __forceinline__ void xcd_barrier(const XcdBarrier& b, int wave) {
;     asm volatile("s_waitcnt vmcnt(0)" ::: "memory");
;     __syncthreads();
;     if (wave == 0 && lane_id_opaque() == 0) {
;         unsigned* bar = b.bar;
;         __builtin_amdgcn_s_waitcnt(0);
;         unsigned nloc = b.st[0], nx = b.st[1];
;         if (nloc == 0u) { xcd_barrier_complete(bar, b.x, nloc, nx); b.st[0] = nloc; b.st[1] = nx; }
;         const unsigned old = xb_add(&bar[XB_XSUB(b.x)], 1u);
.LBB0_2218:
	s_cmp_gt_i32 s89, 14
	s_cselect_b64 s[2:3], -1, 0
	s_and_b64 s[0:1], s[6:7], s[2:3]
	s_andn2_b64 vcc, exec, s[0:1]
	s_cbranch_vccnz .LBB0_2274
	s_setprio 0
	s_waitcnt vmcnt(0) lgkmcnt(0)
	s_barrier
	v_readlane_b32 s0, v254, 45
	s_nop 3
	s_cmp_lg_u32 s0, 0
	s_cbranch_scc1 .Lgb14_end
	s_mov_b64 exec, 1
	v_mov_b32_e32 v0, 0x24160
	ds_read_b64 v[0:1], v0
	v_readlane_b32 s1, v254, 25
	v_readlane_b32 s8, v254, 23
	v_readlane_b32 s9, v254, 24
	s_nop 3
	s_lshl_b32 s1, s1, 8
	s_add_u32 s10, s8, s1
	s_addc_u32 s11, s9, 0
	v_mov_b32_e32 v2, 0x1000
	v_mov_b32_e32 v3, 1
	global_atomic_add v4, v2, v3, s[10:11] offset:1024 sc0
	s_waitcnt vmcnt(0) lgkmcnt(0)
	v_readfirstlane_b32 s12, v4
	v_readfirstlane_b32 s13, v0
	v_readfirstlane_b32 s14, v1
	s_nop 3
	s_mov_b32 s15, 0
	s_max_u32 s13, s13, 1
	s_max_u32 s14, s14, 1

; #define PHASE_IDS(F) const int lane = lane_id_opaque(), wave = (F).wave, tid = wave * 64 + lane; (void)lane; (void)wave; (void)tid
; #define REP(k) _Pragma("unroll 1") for (int rep_ = 0; rep_ < ((((PH_DUP) >> (k)) & 1u) ? 2 : 1); ++rep_)
; #define SEAM(k) do { PH_IDLE(k); if (IN(k) && IN((k) + 1)) xcd_barrier(bar, F.wave); PH_MARK(); } while (0)
; __device__ __forceinline__ void wq_init(Frame& F, WorkQ& Q, gu32* q, int total, int slot, int lane) {
;     Q.q = q; Q.total = total; Q.slot = slot; Q.nxt = 0u;
;     if (F.wave == 0 && lane == 0) Q.nxt = __hip_atomic_fetch_add(q, 1u, RLX_AGENT);
; }
; __device__ __forceinline__ void ret_phase(Frame& F, const Args& A) {
;     PHASE_IDS(F);
;     WorkQ QC; wq_init(F, QC, F.ctl + CW_QC2, CONV_N2 / 64, 18, lane); bool conv_left = true;
;     WorkQ QU; wq_init(F, QU, F.ctl + CW_QRET, 1024, 16, lane);
; __global__ void __launch_bounds__(NWAVES * 64, 2) mk_fwd(Args args) {
;     ...
;     if (IN(14)) REP(14) { ret_phase(F, args); } SEAM(14);
.LBB0_2274:
	s_cmp_lt_i32 s88, 15
	s_cselect_b64 s[0:1], -1, 0
	s_and_b64 s[48:49], s[0:1], s[2:3]
	s_andn2_b64 vcc, exec, s[48:49]
	s_cbranch_vccnz .LBB0_2722
	v_readlane_b32 s0, v254, 45
	s_nop 3
	s_cmp_lt_u32 s0, 4
	s_cbranch_scc1 .Lprio_p34383
	s_setprio 1
.Lprio_p34383:
	s_add_u32 s8, s50, 0x8380
	s_waitcnt vmcnt(0)
	v_mbcnt_lo_u32_b32 v0, -1, 0
	v_mbcnt_hi_u32_b32 v0, -1, v0
	s_addc_u32 s9, s51, 0
	v_or_b32_e32 v1, s87, v0
	v_mov_b32_e32 v132, 0
	v_cmp_ne_u32_e64 s[4:5], 0, v1
	v_cmp_eq_u32_e64 s[2:3], 0, v1
	s_and_saveexec_b64 s[10:11], s[2:3]
	s_cbranch_execz .LBB0_2279
	s_mov_b64 s[14:15], exec
	v_mbcnt_lo_u32_b32 v1, s14, 0
	v_mbcnt_hi_u32_b32 v1, s15, v1
	v_cmp_eq_u32_e32 vcc, 0, v1
	s_and_saveexec_b64 s[12:13], vcc
	s_cbranch_execz .LBB0_2278
	s_bcnt1_i32_b64 s0, s[14:15]
	v_mov_b32_e32 v2, 0
	s_waitcnt lgkmcnt(0)
	v_mov_b32_e32 v3, s0
	global_atomic_add v2, v2, v3, s[8:9] sc0

; __device__ __forceinline__ int lane_id_opaque() { int l; asm volatile("v_mbcnt_lo_u32_b32 %0, -1, 0\n\tv_mbcnt_hi_u32_b32 %0, -1, %0" : "=v"(l)); return l; }
; __device__ __forceinline__ unsigned xb_add(unsigned* p, unsigned v) { return __hip_atomic_fetch_add(p, v, __ATOMIC_RELAXED, __HIP_MEMORY_SCOPE_AGENT); }
; __device__ __forceinline__ void xcd_barrier(const XcdBarrier& b, int wave) {
;     asm volatile("s_waitcnt vmcnt(0)" ::: "memory");
;     __syncthreads();
;     if (wave == 0 && lane_id_opaque() == 0) {
;         unsigned* bar = b.bar;
;         __builtin_amdgcn_s_waitcnt(0);
;         unsigned nloc = b.st[0], nx = b.st[1];
;         if (nloc == 0u) { xcd_barrier_complete(bar, b.x, nloc, nx); b.st[0] = nloc; b.st[1] = nx; }
;         const unsigned old = xb_add(&bar[XB_XSUB(b.x)], 1u);
.LBB0_2722:
	s_cmp_gt_u32 s89, 15
	s_cselect_b64 s[0:1], -1, 0
	s_and_b64 s[0:1], s[48:49], s[0:1]
	s_andn2_b64 vcc, exec, s[0:1]
	v_readlane_b32 s90, v254, 52
	s_cbranch_vccnz .LBB0_2778
	s_setprio 0
	s_waitcnt vmcnt(0) lgkmcnt(0)
	s_barrier
	v_readlane_b32 s0, v254, 45
	s_nop 3
	s_cmp_lg_u32 s0, 0
	s_cbranch_scc1 .Lgb15_end
	s_mov_b64 exec, 1
	v_mov_b32_e32 v0, 0x24160
	ds_read_b64 v[0:1], v0
	v_readlane_b32 s1, v254, 25
	v_readlane_b32 s8, v254, 23
	v_readlane_b32 s9, v254, 24
	s_nop 3
	s_lshl_b32 s1, s1, 8
	s_add_u32 s10, s8, s1
	s_addc_u32 s11, s9, 0
	v_mov_b32_e32 v2, 0x1000
	v_mov_b32_e32 v3, 1
	global_atomic_add v4, v2, v3, s[10:11] offset:1024 sc0
	s_waitcnt vmcnt(0) lgkmcnt(0)
	v_readfirstlane_b32 s12, v4
	v_readfirstlane_b32 s13, v0
	v_readfirstlane_b32 s14, v1
	s_nop 3
	s_mov_b32 s15, 0
	s_max_u32 s13, s13, 1
	s_max_u32 s14, s14, 1

; __device__ __forceinline__ int lane_id_opaque() { int l; asm volatile("v_mbcnt_lo_u32_b32 %0, -1, 0\n\tv_mbcnt_hi_u32_b32 %0, -1, %0" : "=v"(l)); return l; }
; __device__ __forceinline__ unsigned xb_add(unsigned* p, unsigned v) { return __hip_atomic_fetch_add(p, v, __ATOMIC_RELAXED, __HIP_MEMORY_SCOPE_AGENT); }
; __device__ __forceinline__ void xcd_barrier(const XcdBarrier& b, int wave) {
;     asm volatile("s_waitcnt vmcnt(0)" ::: "memory");
;     __syncthreads();
;     if (wave == 0 && lane_id_opaque() == 0) {
;         unsigned* bar = b.bar;
;         __builtin_amdgcn_s_waitcnt(0);
;         unsigned nloc = b.st[0], nx = b.st[1];
;         if (nloc == 0u) { xcd_barrier_complete(bar, b.x, nloc, nx); b.st[0] = nloc; b.st[1] = nx; }
;         const unsigned old = xb_add(&bar[XB_XSUB(b.x)], 1u);
.LBB0_2813:
	s_cmp_gt_i32 s89, 17
	s_cselect_b64 s[2:3], -1, 0
	s_and_b64 s[0:1], s[6:7], s[2:3]
	s_andn2_b64 vcc, exec, s[0:1]
	s_cbranch_vccnz .LBB0_2869
	s_setprio 0
	s_waitcnt vmcnt(0) lgkmcnt(0)
	s_barrier
	v_readlane_b32 s0, v254, 45
	s_nop 3
	s_cmp_lg_u32 s0, 0
	s_cbranch_scc1 .Lgb17_end
	s_mov_b64 exec, 1
	v_mov_b32_e32 v0, 0x24160
	ds_read_b64 v[0:1], v0
	v_readlane_b32 s1, v254, 25
	v_readlane_b32 s8, v254, 23
	v_readlane_b32 s9, v254, 24
	s_nop 3
	s_lshl_b32 s1, s1, 8
	s_add_u32 s10, s8, s1
	s_addc_u32 s11, s9, 0
	v_mov_b32_e32 v2, 0x1000
	v_mov_b32_e32 v3, 1
	global_atomic_add v4, v2, v3, s[10:11] offset:1024 sc0
	s_waitcnt vmcnt(0) lgkmcnt(0)
	v_readfirstlane_b32 s12, v4
	v_readfirstlane_b32 s13, v0
	v_readfirstlane_b32 s14, v1
	s_nop 3
	s_mov_b32 s15, 0
	s_max_u32 s13, s13, 1
	s_max_u32 s14, s14, 1

; __device__ __forceinline__ int lane_id_opaque() { int l; asm volatile("v_mbcnt_lo_u32_b32 %0, -1, 0\n\tv_mbcnt_hi_u32_b32 %0, -1, %0" : "=v"(l)); return l; }
; __device__ __forceinline__ unsigned xb_add(unsigned* p, unsigned v) { return __hip_atomic_fetch_add(p, v, __ATOMIC_RELAXED, __HIP_MEMORY_SCOPE_AGENT); }
; __device__ __forceinline__ void xcd_barrier(const XcdBarrier& b, int wave) {
;     asm volatile("s_waitcnt vmcnt(0)" ::: "memory");
;     __syncthreads();
;     if (wave == 0 && lane_id_opaque() == 0) {
;         unsigned* bar = b.bar;
;         __builtin_amdgcn_s_waitcnt(0);
;         unsigned nloc = b.st[0], nx = b.st[1];
;         if (nloc == 0u) { xcd_barrier_complete(bar, b.x, nloc, nx); b.st[0] = nloc; b.st[1] = nx; }
;         const unsigned old = xb_add(&bar[XB_XSUB(b.x)], 1u);
.LBB0_2927:
	s_cmp_gt_i32 s89, 18
	s_cselect_b64 s[2:3], -1, 0
	s_and_b64 s[0:1], s[30:31], s[2:3]
	s_andn2_b64 vcc, exec, s[0:1]
	s_cbranch_vccnz .LBB0_2983
	s_setprio 0
	s_waitcnt vmcnt(0) lgkmcnt(0)
	s_barrier
	v_readlane_b32 s0, v254, 45
	s_nop 3
	s_cmp_lg_u32 s0, 0
	s_cbranch_scc1 .Lgb18_end
	s_mov_b64 exec, 1
	v_mov_b32_e32 v0, 0x24160
	ds_read_b64 v[0:1], v0
	v_readlane_b32 s1, v254, 25
	v_readlane_b32 s8, v254, 23
	v_readlane_b32 s9, v254, 24
	s_nop 3
	s_lshl_b32 s1, s1, 8
	s_add_u32 s10, s8, s1
	s_addc_u32 s11, s9, 0
	v_mov_b32_e32 v2, 0x1000
	v_mov_b32_e32 v3, 1
	global_atomic_add v4, v2, v3, s[10:11] offset:1024 sc0
	s_waitcnt vmcnt(0) lgkmcnt(0)
	v_readfirstlane_b32 s12, v4
	v_readfirstlane_b32 s13, v0
	v_readfirstlane_b32 s14, v1
	s_nop 3
	s_mov_b32 s15, 0
	s_max_u32 s13, s13, 1
	s_max_u32 s14, s14, 1

; __device__ __forceinline__ int lane_id_opaque() { int l; asm volatile("v_mbcnt_lo_u32_b32 %0, -1, 0\n\tv_mbcnt_hi_u32_b32 %0, -1, %0" : "=v"(l)); return l; }
; __device__ __forceinline__ unsigned xb_add(unsigned* p, unsigned v) { return __hip_atomic_fetch_add(p, v, __ATOMIC_RELAXED, __HIP_MEMORY_SCOPE_AGENT); }
; __device__ __forceinline__ void xcd_barrier(const XcdBarrier& b, int wave) {
;     asm volatile("s_waitcnt vmcnt(0)" ::: "memory");
;     __syncthreads();
;     if (wave == 0 && lane_id_opaque() == 0) {
;         unsigned* bar = b.bar;
;         __builtin_amdgcn_s_waitcnt(0);
;         unsigned nloc = b.st[0], nx = b.st[1];
;         if (nloc == 0u) { xcd_barrier_complete(bar, b.x, nloc, nx); b.st[0] = nloc; b.st[1] = nx; }
;         const unsigned old = xb_add(&bar[XB_XSUB(b.x)], 1u);
.LBB0_3016:
	s_cmp_gt_i32 s89, 19
	s_cselect_b64 s[4:5], -1, 0
	s_and_b64 s[0:1], s[6:7], s[4:5]
	s_andn2_b64 vcc, exec, s[0:1]
	s_cbranch_vccnz .LBB0_3072
	s_setprio 0
	s_waitcnt vmcnt(0) lgkmcnt(0)
	s_barrier
	v_readlane_b32 s0, v254, 45
	s_nop 3
	s_cmp_lg_u32 s0, 0
	s_cbranch_scc1 .Lgb19_end
	s_mov_b64 exec, 1
	v_mov_b32_e32 v0, 0x24160
	ds_read_b64 v[0:1], v0
	v_readlane_b32 s1, v254, 25
	v_readlane_b32 s8, v254, 23
	v_readlane_b32 s9, v254, 24
	s_nop 3
	s_lshl_b32 s1, s1, 8
	s_add_u32 s10, s8, s1
	s_addc_u32 s11, s9, 0
	v_mov_b32_e32 v2, 0x1000
	v_mov_b32_e32 v3, 1
	global_atomic_add v4, v2, v3, s[10:11] offset:1024 sc0
	s_waitcnt vmcnt(0) lgkmcnt(0)
	v_readfirstlane_b32 s12, v4
	v_readfirstlane_b32 s13, v0
	v_readfirstlane_b32 s14, v1
	s_nop 3
	s_mov_b32 s15, 0
	s_max_u32 s13, s13, 1
	s_max_u32 s14, s14, 1

; __device__ __forceinline__ int lane_id_opaque() { int l; asm volatile("v_mbcnt_lo_u32_b32 %0, -1, 0\n\tv_mbcnt_hi_u32_b32 %0, -1, %0" : "=v"(l)); return l; }
; __device__ __forceinline__ unsigned xb_add(unsigned* p, unsigned v) { return __hip_atomic_fetch_add(p, v, __ATOMIC_RELAXED, __HIP_MEMORY_SCOPE_AGENT); }
; __device__ __forceinline__ void xcd_barrier(const XcdBarrier& b, int wave) {
;     asm volatile("s_waitcnt vmcnt(0)" ::: "memory");
;     __syncthreads();
;     if (wave == 0 && lane_id_opaque() == 0) {
;         unsigned* bar = b.bar;
;         __builtin_amdgcn_s_waitcnt(0);
;         unsigned nloc = b.st[0], nx = b.st[1];
;         if (nloc == 0u) { xcd_barrier_complete(bar, b.x, nloc, nx); b.st[0] = nloc; b.st[1] = nx; }
;         const unsigned old = xb_add(&bar[XB_XSUB(b.x)], 1u);
.LBB0_3089:
	s_cmp_gt_i32 s89, 20
	s_cselect_b64 s[4:5], -1, 0
	s_and_b64 s[0:1], s[2:3], s[4:5]
	s_andn2_b64 vcc, exec, s[0:1]
	s_cbranch_vccnz .LBB0_3145
	s_setprio 0
	s_waitcnt vmcnt(0) lgkmcnt(0)
	s_barrier
	v_readlane_b32 s0, v254, 45
	s_nop 3
	s_cmp_lg_u32 s0, 0
	s_cbranch_scc1 .Lgb20_end
	s_mov_b64 exec, 1
	v_mov_b32_e32 v0, 0x24160
	ds_read_b64 v[0:1], v0
	v_readlane_b32 s1, v254, 25
	v_readlane_b32 s8, v254, 23
	v_readlane_b32 s9, v254, 24
	s_nop 3
	s_lshl_b32 s1, s1, 8
	s_add_u32 s10, s8, s1
	s_addc_u32 s11, s9, 0
	v_mov_b32_e32 v2, 0x1000
	v_mov_b32_e32 v3, 1
	global_atomic_add v4, v2, v3, s[10:11] offset:1024 sc0
	s_waitcnt vmcnt(0) lgkmcnt(0)
	v_readfirstlane_b32 s12, v4
	v_readfirstlane_b32 s13, v0
	v_readfirstlane_b32 s14, v1
	s_nop 3
	s_mov_b32 s15, 0
	s_max_u32 s13, s13, 1
	s_max_u32 s14, s14, 1

; __device__ __forceinline__ int lane_id_opaque() { int l; asm volatile("v_mbcnt_lo_u32_b32 %0, -1, 0\n\tv_mbcnt_hi_u32_b32 %0, -1, %0" : "=v"(l)); return l; }
; __device__ __forceinline__ unsigned xb_add(unsigned* p, unsigned v) { return __hip_atomic_fetch_add(p, v, __ATOMIC_RELAXED, __HIP_MEMORY_SCOPE_AGENT); }
; __device__ __forceinline__ void xcd_barrier(const XcdBarrier& b, int wave) {
;     asm volatile("s_waitcnt vmcnt(0)" ::: "memory");
;     __syncthreads();
;     if (wave == 0 && lane_id_opaque() == 0) {
;         unsigned* bar = b.bar;
;         __builtin_amdgcn_s_waitcnt(0);
;         unsigned nloc = b.st[0], nx = b.st[1];
;         if (nloc == 0u) { xcd_barrier_complete(bar, b.x, nloc, nx); b.st[0] = nloc; b.st[1] = nx; }
;         const unsigned old = xb_add(&bar[XB_XSUB(b.x)], 1u);
.LBB0_3199:
	s_cmp_gt_i32 s89, 21
	s_cselect_b64 s[4:5], -1, 0
	s_and_b64 s[0:1], s[2:3], s[4:5]
	s_andn2_b64 vcc, exec, s[0:1]
	s_cbranch_vccnz .LBB0_3255
	s_setprio 0
	s_waitcnt vmcnt(0) lgkmcnt(0)
	s_barrier
	v_readlane_b32 s0, v254, 45
	s_nop 3
	s_cmp_lg_u32 s0, 0
	s_cbranch_scc1 .Lgb21_end
	s_mov_b64 exec, 1
	v_mov_b32_e32 v0, 0x24160
	ds_read_b64 v[0:1], v0
	v_readlane_b32 s1, v254, 25
	v_readlane_b32 s8, v254, 23
	v_readlane_b32 s9, v254, 24
	s_nop 3
	s_lshl_b32 s1, s1, 8
	s_add_u32 s10, s8, s1
	s_addc_u32 s11, s9, 0
	v_mov_b32_e32 v2, 0x1000
	v_mov_b32_e32 v3, 1
	global_atomic_add v4, v2, v3, s[10:11] offset:1024 sc0
	s_waitcnt vmcnt(0) lgkmcnt(0)
	v_readfirstlane_b32 s12, v4
	v_readfirstlane_b32 s13, v0
	v_readfirstlane_b32 s14, v1
	s_nop 3
	s_mov_b32 s15, 0
	s_max_u32 s13, s13, 1
	s_max_u32 s14, s14, 1

; __device__ __forceinline__ int lane_id_opaque() { int l; asm volatile("v_mbcnt_lo_u32_b32 %0, -1, 0\n\tv_mbcnt_hi_u32_b32 %0, -1, %0" : "=v"(l)); return l; }
; __device__ __forceinline__ unsigned xb_add(unsigned* p, unsigned v) { return __hip_atomic_fetch_add(p, v, __ATOMIC_RELAXED, __HIP_MEMORY_SCOPE_AGENT); }
; __device__ __forceinline__ void xcd_barrier(const XcdBarrier& b, int wave) {
;     asm volatile("s_waitcnt vmcnt(0)" ::: "memory");
;     __syncthreads();
;     if (wave == 0 && lane_id_opaque() == 0) {
;         unsigned* bar = b.bar;
;         __builtin_amdgcn_s_waitcnt(0);
;         unsigned nloc = b.st[0], nx = b.st[1];
;         if (nloc == 0u) { xcd_barrier_complete(bar, b.x, nloc, nx); b.st[0] = nloc; b.st[1] = nx; }
;         const unsigned old = xb_add(&bar[XB_XSUB(b.x)], 1u);
.LBB0_3272:
	s_cmp_gt_i32 s89, 22
	s_cselect_b64 s[4:5], -1, 0
	s_and_b64 s[0:1], s[2:3], s[4:5]
	s_andn2_b64 vcc, exec, s[0:1]
	s_cbranch_vccnz .LBB0_3328
	s_setprio 0
	s_waitcnt vmcnt(0) lgkmcnt(0)
	s_barrier
	v_readlane_b32 s0, v254, 45
	s_nop 3
	s_cmp_lg_u32 s0, 0
	s_cbranch_scc1 .Lgb22_end
	s_mov_b64 exec, 1
	v_mov_b32_e32 v0, 0x24160
	ds_read_b64 v[0:1], v0
	v_readlane_b32 s1, v254, 25
	v_readlane_b32 s8, v254, 23
	v_readlane_b32 s9, v254, 24
	s_nop 3
	s_lshl_b32 s1, s1, 8
	s_add_u32 s10, s8, s1
	s_addc_u32 s11, s9, 0
	v_mov_b32_e32 v2, 0x1000
	v_mov_b32_e32 v3, 1
	global_atomic_add v4, v2, v3, s[10:11] offset:1024 sc0
	s_waitcnt vmcnt(0) lgkmcnt(0)
	v_readfirstlane_b32 s12, v4
	v_readfirstlane_b32 s13, v0
	v_readfirstlane_b32 s14, v1
	s_nop 3
	s_mov_b32 s15, 0
	s_max_u32 s13, s13, 1
	s_max_u32 s14, s14, 1
